# speedup vs baseline: 1.0710x; 1.0629x over previous
.Lagg_join_1:
	v_cmp_gt_u32_e32 vcc, s5, v2
	s_and_saveexec_b64 s[58:59], vcc
	v_add_u32_e32 v61, s6, v2
	v_mad_u32_u24 v40, v61, s46, v1
	global_load_dwordx4 v[24:27], v40, s[70:71] nt
	global_load_dwordx4 v[28:31], v40, s[70:71] offset:64 nt
	v_lshlrev_b32_e32 v41, 9, v61
	v_lshl_add_u32 v41, v1, 0, v41
	s_mov_b64 exec, s[58:59]
	s_waitcnt lgkmcnt(0)
	s_barrier
	v_cmp_gt_u32_e32 vcc, s5, v2
	s_and_saveexec_b64 s[58:59], vcc
	v_lshlrev_b32_e32 v61, 2, v0
	v_add_u32_e32 v60, 0x6e40, v61
	ds_read_b32 v48, v61 offset:24448
	ds_read_b32 v49, v61 offset:27584
	ds_read_b32 v50, v61 offset:30720
	ds_read_b32 v51, v61 offset:33856
	ds_read_b32 v52, v61 offset:36992
	ds_read_b32 v53, v61 offset:40128
	ds_read_b32 v54, v61 offset:43264
	ds_read_b32 v55, v61 offset:46400
	ds_read_b32 v45, v61 offset:49536
	s_waitcnt lgkmcnt(0)
	ds_read_b32 v32, v60 offset:24448
	ds_read_b32 v33, v60 offset:27584
	ds_read_b32 v34, v60 offset:30720
	ds_read_b32 v35, v60 offset:33856
	ds_read_b32 v36, v60 offset:36992
	ds_read_b32 v37, v60 offset:40128
	ds_read_b32 v38, v60 offset:43264
	ds_read_b32 v39, v60 offset:46400
	ds_read_b32 v56, v60 offset:49536
	v_mov_b32_e32 v62, 0x3c003c00
	s_waitcnt lgkmcnt(0)
	v_pk_fma_f16 v48, v32, v62, v48
	v_pk_fma_f16 v49, v33, v62, v49
	v_pk_fma_f16 v50, v34, v62, v50
	v_pk_fma_f16 v51, v35, v62, v51
	v_pk_fma_f16 v52, v36, v62, v52
	v_pk_fma_f16 v53, v37, v62, v53
	v_pk_fma_f16 v54, v38, v62, v54
	v_pk_fma_f16 v55, v39, v62, v55
	v_add_f32_e32 v45, v45, v56
	s_cbranch_execz .Lagg_end_1
	v_add_f32_e32 v47, v46, v4
	v_mul_f32_e32 v58, 0x3c23d70a, v47
	v_max_f32_e32 v47, v47, v58
	v_sub_f32_e32 v58, v14, v47
	v_exp_f32_e32 v58, v58
	v_mul_f32_e32 v59, 0x33000000, v45
	v_rcp_f32_e32 v42, v45
	v_mul_f32_e32 v58, 0x24e69595, v58
	v_fma_f32 v60, -v45, v42, 1.0
	v_cmp_ge_f32_e64 s[62:63], v59, v58
	v_cmp_eq_f32_e32 vcc, 0, v45
	v_fmac_f32_e32 v42, v60, v42
	s_nop 1
	v_cndmask_b32_e64 v42, v42, 0, vcc
	s_or_b64 s[62:63], s[62:63], vcc
	s_mov_b64 s[66:67], exec
	s_andn2_b64 exec, exec, s[62:63]
	s_cbranch_execnz .Lagg_gmax_1
.Lagg_gmaxret_1:
	s_mov_b64 exec, s[66:67]
	v_fma_mix_f32 v32, v48, v42, 0 op_sel_hi:[1,0,0]
	v_fma_mix_f32 v33, v48, v42, 0 op_sel:[1,0,0] op_sel_hi:[1,0,0]
	v_fma_mix_f32 v34, v49, v42, 0 op_sel_hi:[1,0,0]
	v_fma_mix_f32 v35, v49, v42, 0 op_sel:[1,0,0] op_sel_hi:[1,0,0]
	v_fma_mix_f32 v36, v50, v42, 0 op_sel_hi:[1,0,0]
	v_fma_mix_f32 v37, v50, v42, 0 op_sel:[1,0,0] op_sel_hi:[1,0,0]
	v_fma_mix_f32 v38, v51, v42, 0 op_sel_hi:[1,0,0]
	v_fma_mix_f32 v39, v51, v42, 0 op_sel:[1,0,0] op_sel_hi:[1,0,0]
	v_fma_mix_f32 v56, v52, v42, 0 op_sel_hi:[1,0,0]
	v_fma_mix_f32 v57, v52, v42, 0 op_sel:[1,0,0] op_sel_hi:[1,0,0]
	v_fma_mix_f32 v58, v53, v42, 0 op_sel_hi:[1,0,0]
	v_fma_mix_f32 v59, v53, v42, 0 op_sel:[1,0,0] op_sel_hi:[1,0,0]
	v_fma_mix_f32 v60, v54, v42, 0 op_sel_hi:[1,0,0]
	v_fma_mix_f32 v61, v54, v42, 0 op_sel:[1,0,0] op_sel_hi:[1,0,0]
	v_fma_mix_f32 v62, v55, v42, 0 op_sel_hi:[1,0,0]
	v_fma_mix_f32 v63, v55, v42, 0 op_sel:[1,0,0] op_sel_hi:[1,0,0]
	v_fma_mix_f32 v32, v5, v15, v32 op_sel_hi:[1,0,0]
	v_fma_mix_f32 v33, v5, v15, v33 op_sel:[1,0,0] op_sel_hi:[1,0,0]
	v_fma_mix_f32 v34, v6, v15, v34 op_sel_hi:[1,0,0]
	v_fma_mix_f32 v35, v6, v15, v35 op_sel:[1,0,0] op_sel_hi:[1,0,0]
	v_fma_mix_f32 v36, v7, v15, v36 op_sel_hi:[1,0,0]
	v_fma_mix_f32 v37, v7, v15, v37 op_sel:[1,0,0] op_sel_hi:[1,0,0]
	v_fma_mix_f32 v38, v8, v15, v38 op_sel_hi:[1,0,0]
	v_fma_mix_f32 v39, v8, v15, v39 op_sel:[1,0,0] op_sel_hi:[1,0,0]
	v_fma_mix_f32 v56, v9, v15, v56 op_sel_hi:[1,0,0]
	v_fma_mix_f32 v57, v9, v15, v57 op_sel:[1,0,0] op_sel_hi:[1,0,0]
	v_fma_mix_f32 v58, v10, v15, v58 op_sel_hi:[1,0,0]
	v_fma_mix_f32 v59, v10, v15, v59 op_sel:[1,0,0] op_sel_hi:[1,0,0]
	v_fma_mix_f32 v60, v11, v15, v60 op_sel_hi:[1,0,0]
	v_fma_mix_f32 v61, v11, v15, v61 op_sel:[1,0,0] op_sel_hi:[1,0,0]
	v_fma_mix_f32 v62, v12, v15, v62 op_sel_hi:[1,0,0]
	v_fma_mix_f32 v63, v12, v15, v63 op_sel:[1,0,0] op_sel_hi:[1,0,0]
	s_waitcnt vmcnt(0)
	v_fma_mix_f32 v32, v24, v15, v32 op_sel_hi:[1,0,0]
	v_fma_mix_f32 v33, v24, v15, v33 op_sel:[1,0,0] op_sel_hi:[1,0,0]
	v_fma_mix_f32 v34, v25, v15, v34 op_sel_hi:[1,0,0]
	v_fma_mix_f32 v35, v25, v15, v35 op_sel:[1,0,0] op_sel_hi:[1,0,0]
	v_fma_mix_f32 v36, v26, v15, v36 op_sel_hi:[1,0,0]
	v_fma_mix_f32 v37, v26, v15, v37 op_sel:[1,0,0] op_sel_hi:[1,0,0]
	v_fma_mix_f32 v38, v27, v15, v38 op_sel_hi:[1,0,0]
	v_fma_mix_f32 v39, v27, v15, v39 op_sel:[1,0,0] op_sel_hi:[1,0,0]
	v_fma_mix_f32 v56, v28, v15, v56 op_sel_hi:[1,0,0]
	v_fma_mix_f32 v57, v28, v15, v57 op_sel:[1,0,0] op_sel_hi:[1,0,0]
	v_fma_mix_f32 v58, v29, v15, v58 op_sel_hi:[1,0,0]
	v_fma_mix_f32 v59, v29, v15, v59 op_sel:[1,0,0] op_sel_hi:[1,0,0]
	v_fma_mix_f32 v60, v30, v15, v60 op_sel_hi:[1,0,0]
	v_fma_mix_f32 v61, v30, v15, v61 op_sel:[1,0,0] op_sel_hi:[1,0,0]
	v_fma_mix_f32 v62, v31, v15, v62 op_sel_hi:[1,0,0]
	v_fma_mix_f32 v63, v31, v15, v63 op_sel:[1,0,0] op_sel_hi:[1,0,0]
	v_max_f32_e32 v32, 0, v32
	v_max_f32_e32 v33, 0, v33
	v_max_f32_e32 v34, 0, v34
	v_max_f32_e32 v35, 0, v35
	v_max_f32_e32 v36, 0, v36
	v_max_f32_e32 v37, 0, v37
	v_max_f32_e32 v38, 0, v38
	v_max_f32_e32 v39, 0, v39
	v_max_f32_e32 v56, 0, v56
	v_max_f32_e32 v57, 0, v57
	v_max_f32_e32 v58, 0, v58
	v_max_f32_e32 v59, 0, v59
	v_max_f32_e32 v60, 0, v60
	v_max_f32_e32 v61, 0, v61
	v_max_f32_e32 v62, 0, v62
	v_max_f32_e32 v63, 0, v63
	v_lshlrev_b32_e32 v40, 2, v0
	v_add_u32_e32 v44, 0x6200, v40
	ds_write_b32 v40, v32 offset:24448
	ds_write_b32 v40, v33 offset:27584
	ds_write_b32 v40, v34 offset:30720
	ds_write_b32 v40, v35 offset:33856
	ds_write_b32 v40, v36 offset:36992
	ds_write_b32 v40, v37 offset:40128
	ds_write_b32 v40, v38 offset:43264
	ds_write_b32 v40, v39 offset:46400
	ds_write_b32 v44, v56 offset:24448
	ds_write_b32 v44, v57 offset:27584
	ds_write_b32 v44, v58 offset:30720
	ds_write_b32 v44, v59 offset:33856
	ds_write_b32 v44, v60 offset:36992
	ds_write_b32 v44, v61 offset:40128
	ds_write_b32 v44, v62 offset:43264
	ds_write_b32 v44, v63 offset:46400
	v_lshrrev_b32_e32 v42, 4, v1
	v_mul_u32_u24_e32 v42, 0x3100, v42
	v_and_b32_e32 v43, -4, v0
	v_lshl_add_u32 v42, v43, 2, v42
	s_waitcnt lgkmcnt(0)
	ds_read_b32 v32, v42 offset:24448
	ds_read_b32 v33, v42 offset:27584
	ds_read_b32 v34, v42 offset:30720
	ds_read_b32 v35, v42 offset:33856
	ds_read_b32 v36, v42 offset:24452
	ds_read_b32 v37, v42 offset:27588
	ds_read_b32 v38, v42 offset:30724
	ds_read_b32 v39, v42 offset:33860
	ds_read_b32 v56, v42 offset:24456
	ds_read_b32 v57, v42 offset:27592
	ds_read_b32 v58, v42 offset:30728
	ds_read_b32 v59, v42 offset:33864
	ds_read_b32 v60, v42 offset:24460
	ds_read_b32 v61, v42 offset:27596
	ds_read_b32 v62, v42 offset:30732
	ds_read_b32 v63, v42 offset:33868
	s_waitcnt lgkmcnt(0)
	global_store_dwordx4 v41, v[32:35], s[68:69] nt
	global_store_dwordx4 v41, v[36:39], s[68:69] offset:64 nt
	global_store_dwordx4 v41, v[56:59], s[68:69] offset:128 nt
	global_store_dwordx4 v41, v[60:63], s[68:69] offset:192 nt
	s_nop 1
